# speedup vs baseline: 1.0057x; 1.0057x over previous
.LBB1_3:
	s_load_dwordx8 s[4:11], s[0:1], 0x8
	s_lshr_b32 s16, s13, 6
	s_mul_i32 s14, s16, 0x1800
	s_mov_b32 s15, 0
	s_lshl_b64 s[18:19], s[14:15], 4
	v_and_b32_e32 v2, 63, v0
	s_waitcnt lgkmcnt(0)
	s_lshl_b32 s24, s12, 7
	s_add_u32 s21, s6, s24
	s_add_u32 s22, s8, s24
	s_add_u32 s23, s10, s24
	s_sub_u32 s21, s21, 0x20100
	s_sub_u32 s22, s22, 0x22100
	s_sub_u32 s23, s23, 0x24100
	s_add_u32 s4, s4, s18
	s_addc_u32 s5, s5, s19
	v_lshlrev_b32_e32 v54, 4, v2
	v_mov_b32_e32 v55, 0
	v_lshl_add_u64 v[18:19], s[4:5], 0, v[54:55]
	s_bfe_u32 s4, s2, 0x40003
	s_mul_i32 s14, s4, 0x1800
	v_lshl_add_u64 v[20:21], v[18:19], 0, s[14:15]
	global_load_dwordx4 v[2:5], v[20:21], off offset:2048
	global_load_dwordx4 v[6:9], v[20:21], off
	global_load_dwordx4 v[10:13], v[20:21], off offset:1024
	v_lshrrev_b32_e32 v14, 1, v0
	v_bfe_u32 v56, v0, 4, 2
	v_lshlrev_b32_e32 v54, 7, v1
	v_bitop3_b32 v14, v56, v14, 7 bitop3:0x78
	v_lshl_or_b32 v57, v14, 4, v54
	global_load_dwordx4 v[14:17], v[20:21], off offset:3072
	s_movk_i32 s2, 0x1000
	s_add_i32 s5, s3, 1
	s_and_b32 s5, s5, 15
	v_add_co_u32_e32 v44, vcc, s2, v20
	s_mul_i32 s14, s5, 0x1800
	s_nop 0
	v_addc_co_u32_e32 v45, vcc, 0, v21, vcc
	v_lshl_add_u64 v[46:47], v[18:19], 0, s[14:15]
	global_load_dwordx4 v[20:23], v[44:45], off
	global_load_dwordx4 v[24:27], v[44:45], off offset:1024
	global_load_dwordx4 v[28:31], v[46:47], off
	global_load_dwordx4 v[32:35], v[46:47], off offset:1024
	global_load_dwordx4 v[36:39], v[46:47], off offset:2048
	global_load_dwordx4 v[40:43], v[46:47], off offset:3072
	s_add_i32 s13, s3, 2
	s_and_b32 s13, s13, 15
	v_add_co_u32_e32 v52, vcc, s2, v46
	s_mul_i32 s14, s13, 0x1800
	s_nop 0
	v_addc_co_u32_e32 v53, vcc, 0, v47, vcc
	v_lshl_add_u64 v[58:59], v[18:19], 0, s[14:15]
	global_load_dwordx4 v[44:47], v[52:53], off
	global_load_dwordx4 v[48:51], v[52:53], off offset:1024
	global_load_dwordx4 v[60:63], v[58:59], off
	global_load_dwordx4 v[64:67], v[58:59], off offset:1024
	global_load_dwordx4 v[68:71], v[58:59], off offset:2048
	global_load_dwordx4 v[72:75], v[58:59], off offset:3072
	v_add_co_u32_e32 v52, vcc, s2, v58
	s_add_i32 s5, s3, 3
	s_nop 0
	v_addc_co_u32_e32 v53, vcc, 0, v59, vcc
	global_load_dwordx4 v[76:79], v[52:53], off
	global_load_dwordx4 v[80:83], v[52:53], off offset:1024

.Lproj_go_15:
	s_waitcnt vmcnt(8)
	v_mfma_f32_16x16x32_f16 v[100:103], v[10:13], v[116:119], v[100:103]
	ds_read_b128 v[128:131], v59
	ds_read_b128 v[132:135], v132
	v_or_b32_e32 v59, 0x1f000, v57
	v_or_b32_e32 v57, 0x1f800, v57
	s_waitcnt vmcnt(7)
	v_mfma_f32_16x16x32_f16 v[104:107], v[6:9], v[116:119], v[104:107]
	ds_read_b128 v[136:139], v59
	ds_read_b128 v[140:143], v57
	v_or_b32_e32 v57, 0x1e000, v58
	v_or_b32_e32 v59, 0x1e800, v58
	s_waitcnt vmcnt(6)
	v_mfma_f32_16x16x32_f16 v[68:71], v[116:119], v[2:5], v[68:71]
	ds_read_b128 v[116:119], v57
	ds_read_b128 v[144:147], v59
	v_or_b32_e32 v57, 0x1f000, v58
	v_or_b32_e32 v58, 0x1f800, v58
	s_waitcnt vmcnt(5) lgkmcnt(5)
	v_mfma_f32_16x16x32_f16 v[100:103], v[38:41], v[128:131], v[100:103]
	ds_read_b128 v[148:151], v57
	ds_read_b128 v[152:155], v58
	v_lshl_add_u64 v[58:59], s[4:5], 0, v[54:55]
	v_and_b32_e32 v54, 48, v0
	s_waitcnt vmcnt(4)
	v_mfma_f32_16x16x32_f16 v[104:107], v[34:37], v[128:131], v[104:107]
	s_lshl_b32 s4, s16, 5
	s_waitcnt vmcnt(3)
	v_mfma_f32_16x16x32_f16 v[68:71], v[128:131], v[30:33], v[68:71]
	v_lshl_add_u64 v[128:129], v[58:59], 0, v[54:55]
	s_waitcnt vmcnt(2) lgkmcnt(3)
	v_mfma_f32_16x16x32_f16 v[100:103], v[22:25], v[116:119], v[100:103]
	s_waitcnt vmcnt(1)
	v_mfma_f32_16x16x32_f16 v[104:107], v[26:29], v[116:119], v[104:107]
	s_waitcnt vmcnt(0)
	v_mfma_f32_16x16x32_f16 v[68:71], v[116:119], v[18:21], v[68:71]
	s_nop 3
	v_mov_b32_e32 v54, v101
	v_mov_b32_e32 v55, v102
	v_pk_mul_f32 v[54:55], v[54:55], s[2:3] op_sel_hi:[1,0]
	v_mfma_f32_16x16x32_f16 v[76:79], v[10:13], v[120:123], v[76:79]
	v_fma_mixlo_f16 v57, v100, s2, 0
	v_cvt_pk_f16_f32 v100, v54, v55
	v_mov_b32_e32 v54, v105
	v_mov_b32_e32 v55, v106
	v_mfma_f32_16x16x32_f16 v[84:87], v[6:9], v[120:123], v[84:87]
	v_mul_f32_e64 v54, v54, s2
	v_mul_f32_e64 v55, v55, s2
	v_pack_b32_f16 v58, v57, v100
	v_cvt_pk_f16_f32 v57, v54, v55
	v_mov_b32_e32 v54, v69
	v_mfma_f32_16x16x32_f16 v[88:91], v[120:123], v[2:5], v[88:91]
	v_mov_b32_e32 v55, v70
	v_pk_mul_f32 v[54:55], v[54:55], s[2:3] op_sel_hi:[1,0]
	v_fma_mixlo_f16 v59, v104, s2, 0
	v_mfma_f32_16x16x32_f16 v[76:79], v[38:41], v[132:135], v[76:79]
	v_cvt_pk_f16_f32 v70, v54, v55
	v_fma_mixlo_f16 v54, v103, s2, 0
	v_fma_mixlo_f16 v104, v68, s2, 0
	v_mfma_f32_16x16x32_f16 v[84:87], v[34:37], v[132:135], v[84:87]
	v_pack_b32_f16 v68, v59, v57
	v_alignbit_b32 v59, v54, v100, 16
	v_fma_mixlo_f16 v54, v107, s2, 0
	v_alignbit_b32 v69, v54, v57, 16
	v_lshlrev_b64 v[100:101], 7, v[156:157]
	v_mfma_f32_16x16x32_f16 v[88:91], v[132:135], v[30:33], v[88:91]
	v_lshl_or_b32 v105, v56, 3, s4
	v_or_b32_e32 v100, v100, v105
	v_lshl_add_u64 v[102:103], s[6:7], 0, v[100:101]
	s_waitcnt lgkmcnt(2)
	v_mfma_f32_16x16x32_f16 v[54:57], v[22:25], v[144:147], v[76:79]
	v_subrev_u32_e32 v170, s21, v102
	ds_write_b64 v170, v[58:59]
	v_lshl_add_u64 v[58:59], s[8:9], 0, v[100:101]
	v_subrev_u32_e32 v170, s22, v58
	ds_write_b64 v170, v[68:69]
	v_mfma_f32_16x16x32_f16 v[76:79], v[26:29], v[144:147], v[84:87]
	v_or_b32_e32 v68, 16, v156
	s_nop 2
	v_fma_mixlo_f16 v58, v54, s2, 0
	v_mov_b32_e32 v54, v55
	v_mfma_f32_16x16x32_f16 v[84:87], v[144:147], v[18:21], v[88:91]
	v_mov_b32_e32 v55, v56
	v_pk_mul_f32 v[54:55], v[54:55], s[2:3] op_sel_hi:[1,0]
	v_fma_mixlo_f16 v59, v76, s2, 0
	v_mfma_f32_16x16x32_f16 v[60:63], v[46:49], v[80:83], v[60:63]
	v_cvt_pk_f16_f32 v56, v54, v55
	v_mov_b32_e32 v54, v77
	v_mov_b32_e32 v55, v78
	v_mfma_f32_16x16x32_f16 v[72:75], v[42:45], v[80:83], v[72:75]
	v_mul_f32_e64 v54, v54, s2
	v_mul_f32_e64 v55, v55, s2
	v_pack_b32_f16 v76, v58, v56
	v_ashrrev_i32_e32 v69, 31, v68
	v_mfma_f32_16x16x32_f16 v[80:83], v[80:83], v[14:17], v[92:95]
	v_lshlrev_b64 v[68:69], 7, v[68:69]
	v_or_b32_e32 v68, v68, v105
	v_fma_mixlo_f16 v84, v84, s2, 0
	v_mfma_f32_16x16x32_f16 v[42:45], v[42:45], v[112:115], v[64:67]
	s_nop 2
	v_cvt_pk_f16_f32 v67, v54, v55
	v_mov_b32_e32 v54, v85
	v_mov_b32_e32 v55, v86
	v_pk_mul_f32 v[54:55], v[54:55], s[2:3] op_sel_hi:[1,0]
	v_pack_b32_f16 v66, v59, v67
	v_mfma_f32_16x16x32_f16 v[58:61], v[10:13], v[96:99], v[60:63]
	v_mfma_f32_16x16x32_f16 v[62:65], v[6:9], v[96:99], v[72:75]
	s_nop 2
	v_cvt_pk_f16_f32 v74, v54, v55
	v_fma_mixlo_f16 v54, v57, s2, 0
	v_alignbit_b32 v77, v54, v56, 16
	v_mfma_f32_16x16x32_f16 v[54:57], v[96:99], v[2:5], v[80:83]
	v_fma_mixlo_f16 v72, v79, s2, 0
	v_alignbit_b32 v67, v72, v67, 16
	v_lshl_add_u64 v[72:73], s[6:7], 0, v[68:69]
	v_mfma_f32_16x16x32_f16 v[46:49], v[46:49], v[112:115], v[108:111]
	v_lshl_add_u64 v[68:69], s[8:9], 0, v[68:69]
	v_subrev_u32_e32 v170, s22, v68
	ds_write_b64 v170, v[66:67]
	v_lshrrev_b32_e32 v67, 16, v70
	v_mfma_f32_16x16x32_f16 v[58:61], v[38:41], v[136:139], v[58:61]
	v_lshrrev_b32_e32 v69, 16, v74
	v_fma_mixhi_f16 v69, v87, s2, 0
	v_fma_mixhi_f16 v67, v71, s2, 0
	v_mfma_f32_16x16x32_f16 v[54:57], v[136:139], v[30:33], v[54:57]
	v_pack_b32_f16 v68, v84, v74
	v_pack_b32_f16 v66, v104, v70
	v_subrev_u32_e32 v170, s23, v128
	ds_write_b128 v170, v[66:69]
	v_mfma_f32_16x16x32_f16 v[62:65], v[34:37], v[136:139], v[62:65]
	v_subrev_u32_e32 v170, s21, v72
	ds_write_b64 v170, v[76:77]
	v_or_b32_e32 v66, 32, v156
	v_ashrrev_i32_e32 v67, 31, v66
	v_mfma_f32_16x16x32_f16 v[14:17], v[112:115], v[14:17], v[50:53]
	v_mfma_f32_16x16x32_f16 v[6:9], v[6:9], v[124:127], v[42:45]
	s_waitcnt lgkmcnt(1)
	v_mfma_f32_16x16x32_f16 v[58:61], v[22:25], v[148:151], v[58:61]
	v_mfma_f32_16x16x32_f16 v[54:57], v[148:151], v[18:21], v[54:57]
	v_mfma_f32_16x16x32_f16 v[10:13], v[10:13], v[124:127], v[46:49]
	s_nop 5
	v_fma_mixlo_f16 v68, v58, s2, 0
	v_mov_b32_e32 v58, v59
	v_mov_b32_e32 v59, v60
	v_mfma_f32_16x16x32_f16 v[62:65], v[26:29], v[148:151], v[62:65]
	v_mul_f32_e64 v50, v58, s2
	v_mul_f32_e64 v51, v59, s2
	v_fma_mixlo_f16 v54, v54, s2, 0
	v_cvt_pk_f16_f32 v50, v50, v51
	v_mfma_f32_16x16x32_f16 v[2:5], v[124:127], v[2:5], v[14:17]
	v_pack_b32_f16 v46, v68, v50
	s_nop 1
	v_mov_b32_e32 v48, v63
	v_mov_b32_e32 v49, v64
	v_mfma_f32_16x16x32_f16 v[6:9], v[34:37], v[140:143], v[6:9]
	v_mov_b32_e32 v14, v55
	v_mov_b32_e32 v15, v56
	v_pk_mul_f32 v[14:15], v[14:15], s[2:3] op_sel_hi:[1,0]
	v_mfma_f32_16x16x32_f16 v[10:13], v[38:41], v[140:143], v[10:13]
	v_mul_f32_e64 v42, v48, s2
	v_mul_f32_e64 v43, v49, s2
	v_cvt_pk_f16_f32 v38, v14, v15
	v_fma_mixlo_f16 v14, v61, s2, 0
	v_mfma_f32_16x16x32_f16 v[2:5], v[140:143], v[30:33], v[2:5]
	v_fma_mixlo_f16 v62, v62, s2, 0
	v_cvt_pk_f16_f32 v43, v42, v43
	v_alignbit_b32 v47, v14, v50, 16
	v_fma_mixlo_f16 v14, v65, s2, 0
	s_waitcnt lgkmcnt(0)
	v_mfma_f32_16x16x32_f16 v[6:9], v[26:29], v[152:155], v[6:9]
	v_pack_b32_f16 v42, v62, v43
	v_alignbit_b32 v43, v14, v43, 16
	v_lshlrev_b64 v[14:15], 7, v[66:67]
	v_mfma_f32_16x16x32_f16 v[10:13], v[22:25], v[152:155], v[10:13]
	v_or_b32_e32 v14, v14, v105
	v_lshl_add_u64 v[16:17], s[6:7], 0, v[14:15]
	v_subrev_u32_e32 v170, s21, v16
	ds_write_b64 v170, v[46:47]
	v_mfma_f32_16x16x32_f16 v[2:5], v[152:155], v[18:21], v[2:5]
	v_lshl_add_u64 v[14:15], s[8:9], 0, v[14:15]
	v_fma_mixlo_f16 v17, v6, s2, 0
	v_mov_b32_e32 v6, v7
	v_mov_b32_e32 v7, v8
	v_subrev_u32_e32 v170, s22, v14
	ds_write_b64 v170, v[42:43]
	v_or_b32_e32 v14, 48, v156
	v_fma_mixlo_f16 v16, v10, s2, 0
	v_mov_b32_e32 v10, v11
	v_mov_b32_e32 v11, v12
	v_pk_mul_f32 v[6:7], v[6:7], s[2:3] op_sel_hi:[1,0]
	v_ashrrev_i32_e32 v15, 31, v14
	v_pk_mul_f32 v[10:11], v[10:11], s[2:3] op_sel_hi:[1,0]
	v_cvt_pk_f16_f32 v7, v6, v7
	v_fma_mixlo_f16 v8, v9, s2, 0
	v_cvt_pk_f16_f32 v12, v10, v11
	v_pack_b32_f16 v6, v17, v7
	v_mov_b32_e32 v10, v3
	v_mov_b32_e32 v11, v4
	v_alignbit_b32 v7, v8, v7, 16
	v_lshlrev_b64 v[8:9], 7, v[14:15]
	v_pk_mul_f32 v[10:11], v[10:11], s[2:3] op_sel_hi:[1,0]
	v_fma_mixlo_f16 v3, v13, s2, 0
	v_or_b32_e32 v8, v8, v105
	v_fma_mixlo_f16 v18, v2, s2, 0
	v_pack_b32_f16 v2, v16, v12
	v_cvt_pk_f16_f32 v4, v10, v11
	v_alignbit_b32 v3, v3, v12, 16
	v_lshl_add_u64 v[10:11], s[6:7], 0, v[8:9]
	v_subrev_u32_e32 v170, s21, v10
	ds_write_b64 v170, v[2:3]
	v_lshl_add_u64 v[2:3], s[8:9], 0, v[8:9]
	v_subrev_u32_e32 v170, s22, v2
	ds_write_b64 v170, v[6:7]
	v_lshrrev_b32_e32 v7, 16, v38
	v_lshrrev_b32_e32 v9, 16, v4
	v_fma_mixhi_f16 v9, v5, s2, 0
	v_fma_mixhi_f16 v7, v57, s2, 0
	v_pack_b32_f16 v8, v18, v4
	v_pack_b32_f16 v6, v54, v38
	v_subrev_u32_e32 v170, s23, v128
	ds_write_b128 v170, v[6:9] offset:64
	s_waitcnt lgkmcnt(0)
	s_barrier
	v_and_b32_e32 v170, 63, v0
	v_lshlrev_b32_e32 v170, 4, v170
	v_lshl_add_u32 v170, s16, 10, v170
	v_add_u32_e32 v168, s24, v170
	v_add_u32_e32 v169, 0x1000, v168
	v_add_u32_e32 v170, 0x20100, v170
	ds_read_b128 v[160:163], v170
	ds_read_b128 v[164:167], v170 offset:4096
	ds_read_b128 v[172:175], v170 offset:8192
	s_waitcnt lgkmcnt(2)
	global_store_dwordx4 v168, v[160:163], s[6:7] sc1
	s_waitcnt lgkmcnt(1)
	global_store_dwordx4 v169, v[164:167], s[6:7] sc1
	s_waitcnt lgkmcnt(0)
	global_store_dwordx4 v168, v[172:175], s[8:9] sc1
	s_nop 1
	ds_read_b128 v[160:163], v170 offset:12288
	ds_read_b128 v[164:167], v170 offset:16384
	ds_read_b128 v[172:175], v170 offset:20480
	s_waitcnt lgkmcnt(2)
	global_store_dwordx4 v169, v[160:163], s[8:9] sc1
	s_waitcnt lgkmcnt(1)
	global_store_dwordx4 v168, v[164:167], s[10:11] sc1
	s_waitcnt lgkmcnt(0)
	global_store_dwordx4 v169, v[172:175], s[10:11] sc1
	s_endpgm

	.amdhsa_kernel _Z11proj_kernelPKfPKDv8_DF16_PDF16_S4_S4_
		.amdhsa_group_segment_fixed_size 155904
		.amdhsa_private_segment_fixed_size 0
		.amdhsa_kernarg_size 40
		.amdhsa_user_sgpr_count 2
		.amdhsa_user_sgpr_dispatch_ptr 0
		.amdhsa_user_sgpr_queue_ptr 0
		.amdhsa_user_sgpr_kernarg_segment_ptr 1
		.amdhsa_user_sgpr_dispatch_id 0
		.amdhsa_user_sgpr_kernarg_preload_length 0
		.amdhsa_user_sgpr_kernarg_preload_offset 0
		.amdhsa_user_sgpr_private_segment_size 0
		.amdhsa_uses_dynamic_stack 0
		.amdhsa_enable_private_segment 0
		.amdhsa_system_sgpr_workgroup_id_x 1
		.amdhsa_system_sgpr_workgroup_id_y 0
		.amdhsa_system_sgpr_workgroup_id_z 0
		.amdhsa_system_sgpr_workgroup_info 0
		.amdhsa_system_vgpr_workitem_id 0
		.amdhsa_next_free_vgpr 176
		.amdhsa_next_free_sgpr 96
		.amdhsa_accum_offset 176
		.amdhsa_reserve_vcc 1
		.amdhsa_float_round_mode_32 0
		.amdhsa_float_round_mode_16_64 0
		.amdhsa_float_denorm_mode_32 3
		.amdhsa_float_denorm_mode_16_64 3
		.amdhsa_dx10_clamp 1
		.amdhsa_ieee_mode 1
		.amdhsa_fp16_overflow 0
		.amdhsa_tg_split 0
		.amdhsa_exception_fp_ieee_invalid_op 0
		.amdhsa_exception_fp_denorm_src 0
		.amdhsa_exception_fp_ieee_div_zero 0
		.amdhsa_exception_fp_ieee_overflow 0
		.amdhsa_exception_fp_ieee_underflow 0
		.amdhsa_exception_fp_ieee_inexact 0
		.amdhsa_exception_int_div_zero 0
	.end_amdhsa_kernel

amdhsa.kernels:
  - .agpr_count:     0
    .args:
      - .actual_access:  read_only
        .address_space:  global
        .offset:         0
        .size:           8
        .value_kind:     global_buffer
      - .actual_access:  read_only
        .address_space:  global
        .offset:         8
        .size:           8
        .value_kind:     global_buffer
      - .actual_access:  read_only
        .address_space:  global
        .offset:         16
        .size:           8
        .value_kind:     global_buffer
      - .actual_access:  write_only
        .address_space:  global
        .offset:         24
        .size:           8
        .value_kind:     global_buffer
      - .offset:         32
        .size:           4
        .value_kind:     hidden_block_count_x
      - .offset:         36
        .size:           4
        .value_kind:     hidden_block_count_y
      - .offset:         40
        .size:           4
        .value_kind:     hidden_block_count_z
      - .offset:         44
        .size:           2
        .value_kind:     hidden_group_size_x
      - .offset:         46
        .size:           2
        .value_kind:     hidden_group_size_y
      - .offset:         48
        .size:           2
        .value_kind:     hidden_group_size_z
      - .offset:         50
        .size:           2
        .value_kind:     hidden_remainder_x
      - .offset:         52
        .size:           2
        .value_kind:     hidden_remainder_y
      - .offset:         54
        .size:           2
        .value_kind:     hidden_remainder_z
      - .offset:         72
        .size:           8
        .value_kind:     hidden_global_offset_x
      - .offset:         80
        .size:           8
        .value_kind:     hidden_global_offset_y
      - .offset:         88
        .size:           8
        .value_kind:     hidden_global_offset_z
      - .offset:         96
        .size:           2
        .value_kind:     hidden_grid_dims
    .group_segment_fixed_size: 0
    .kernarg_segment_align: 8
    .kernarg_segment_size: 288
    .language:       OpenCL C
    .language_version:
      - 2
      - 0
    .max_flat_workgroup_size: 1024
    .name:           _Z13prep_w_kernelPKfS0_S0_PDv8_DF16_
    .private_segment_fixed_size: 0
    .sgpr_count:     18
    .sgpr_spill_count: 0
    .symbol:         _Z13prep_w_kernelPKfS0_S0_PDv8_DF16_.kd
    .uniform_work_group_size: 1
    .uses_dynamic_stack: false
    .vgpr_count:     15
    .vgpr_spill_count: 0
    .wavefront_size: 64
  - .agpr_count:     0
    .args:
      - .actual_access:  read_only
        .address_space:  global
        .offset:         0
        .size:           8
        .value_kind:     global_buffer
      - .actual_access:  read_only
        .address_space:  global
        .offset:         8
        .size:           8
        .value_kind:     global_buffer
      - .actual_access:  write_only
        .address_space:  global
        .offset:         16
        .size:           8
        .value_kind:     global_buffer
      - .actual_access:  write_only
        .address_space:  global
        .offset:         24
        .size:           8
        .value_kind:     global_buffer
      - .actual_access:  write_only
        .address_space:  global
        .offset:         32
        .size:           8
        .value_kind:     global_buffer
    .group_segment_fixed_size: 155904
    .kernarg_segment_align: 8
    .kernarg_segment_size: 40
    .language:       OpenCL C
    .language_version:
      - 2
      - 0
    .max_flat_workgroup_size: 512
    .name:           _Z11proj_kernelPKfPKDv8_DF16_PDF16_S4_S4_
    .private_segment_fixed_size: 0
    .sgpr_count:     26
    .sgpr_spill_count: 0
    .symbol:         _Z11proj_kernelPKfPKDv8_DF16_PDF16_S4_S4_.kd
    .uniform_work_group_size: 1
    .uses_dynamic_stack: false
    .vgpr_count:     176
    .vgpr_spill_count: 0
    .wavefront_size: 64
  - .agpr_count:     0
    .args:
      - .actual_access:  read_only
        .address_space:  global
        .offset:         0
        .size:           8
        .value_kind:     global_buffer
      - .address_space:  global
        .offset:         8
        .size:           8
        .value_kind:     global_buffer
      - .address_space:  global
        .offset:         16
        .size:           8
        .value_kind:     global_buffer
      - .actual_access:  write_only
        .address_space:  global
        .offset:         24
        .size:           8
        .value_kind:     global_buffer
      - .actual_access:  write_only
        .address_space:  global
        .offset:         32
        .size:           8
        .value_kind:     global_buffer
      - .actual_access:  write_only
        .address_space:  global
        .offset:         40
        .size:           8
        .value_kind:     global_buffer
    .group_segment_fixed_size: 65536
    .kernarg_segment_align: 8
    .kernarg_segment_size: 48
    .language:       OpenCL C
    .language_version:
      - 2
      - 0
    .max_flat_workgroup_size: 512
    .name:           _Z11attn_kernelPKDF16_S0_S0_PfPDF16_S1_
    .private_segment_fixed_size: 0
    .sgpr_count:     96
    .sgpr_spill_count: 0
    .symbol:         _Z11attn_kernelPKDF16_S0_S0_PfPDF16_S1_.kd
    .uniform_work_group_size: 1
    .uses_dynamic_stack: false
    .vgpr_count:     120
    .vgpr_spill_count: 0
    .wavefront_size: 64
  - .agpr_count:     0
    .args:
      - .actual_access:  read_only
        .address_space:  global
        .offset:         0
        .size:           8
        .value_kind:     global_buffer
      - .actual_access:  read_only
        .address_space:  global
        .offset:         8
        .size:           8
        .value_kind:     global_buffer
      - .actual_access:  write_only
        .address_space:  global
        .offset:         16
        .size:           8
        .value_kind:     global_buffer
    .group_segment_fixed_size: 0
    .kernarg_segment_align: 8
    .kernarg_segment_size: 24
    .language:       OpenCL C
    .language_version:
      - 2
      - 0
    .max_flat_workgroup_size: 256
    .name:           _Z14combine_kernelPKDF16_PKfPf
    .private_segment_fixed_size: 0
    .sgpr_count:     70
    .sgpr_spill_count: 0
    .symbol:         _Z14combine_kernelPKDF16_PKfPf.kd
    .uniform_work_group_size: 1
    .uses_dynamic_stack: false
    .vgpr_count:     46
    .vgpr_spill_count: 0
    .wavefront_size: 64
